# v12 + post and prep work assigned by sequence (XCD x = sequence x) with XCD-local barriers for post->branch and z GEMM->prep
# speedup vs baseline: 1.0423x; 1.0023x over previous
.LBB0_821:
	s_or_b64 exec, exec, s[12:13]
	s_cmpk_lt_i32 s93, 0x400
	s_waitcnt vmcnt(0)
	ds_write_b32 v5, v6 offset:34816
	s_waitcnt lgkmcnt(0)
	s_barrier
	s_cbranch_scc0 .LBB0_899
	s_add_u32 s12, s6, 0x48000000
	s_addc_u32 s13, s7, 0
	s_add_u32 s14, s6, 0x64000000
	s_addc_u32 s15, s7, 0
	s_add_u32 s16, s6, 0x70200000
	v_readlane_b32 s20, v255, 4
	s_addc_u32 s17, s7, 0
	v_readlane_b32 s21, v255, 5
	s_mul_i32 s18, s20, 0x48000
	s_mov_b32 s21, s35
	s_mul_hi_u32 s5, s20, 0x48000
	s_add_u32 s24, s6, s18
	s_mov_b32 s18, s20
	s_addc_u32 s25, s7, s5
	v_writelane_b32 v255, s18, 4
	s_lshl_b64 s[26:27], s[20:21], 17
	v_ashrrev_i32_e32 v1, 4, v4
	v_writelane_b32 v255, s19, 5
	s_add_u32 s18, s6, 0x5e000000
	s_addc_u32 s19, s7, 0
	s_add_u32 s20, s6, 0x6c200000
	v_lshlrev_b32_e32 v2, 2, v4
	s_addc_u32 s21, s7, 0
	v_and_b32_e32 v5, 48, v2
	v_lshlrev_b32_e32 v2, 3, v1
	s_add_u32 s22, s6, 0x6e200000
	v_ashrrev_i32_e32 v3, 31, v2
	s_addc_u32 s23, s7, 0
	v_lshlrev_b64 v[2:3], 1, v[2:3]
	s_add_u32 s26, s6, s26
	v_lshl_add_u64 v[6:7], s[24:25], 0, v[2:3]
	s_mov_b64 s[24:25], 0x7c00000
	v_and_b32_e32 v127, 15, v4
	s_addc_u32 s27, s7, s27
	v_lshl_add_u64 v[130:131], v[6:7], 0, s[24:25]
	s_movk_i32 s24, 0x250
	s_ashr_i32 s83, s82, 31
	s_ashr_i32 s5, s4, 31
	v_mad_u32_u24 v9, v127, s24, 0
	s_lshl_b64 s[24:25], s[82:83], 2
	s_add_u32 s24, s6, s24
	s_addc_u32 s25, s7, s25
	s_add_u32 s24, s24, 0x6c000000
	s_addc_u32 s25, s25, 0
	s_add_u32 s52, s6, 0x5f000000
	s_addc_u32 s53, s7, 0
	s_add_u32 s54, s6, 0x60000000
	s_addc_u32 s55, s7, 0
	s_add_u32 s56, s6, 0x61000000
	s_addc_u32 s57, s7, 0
	s_add_u32 s58, s6, 0x62000000
	s_addc_u32 s59, s7, 0
	s_add_u32 s60, s6, 0x63000000
	s_addc_u32 s61, s7, 0
	s_lshl_b64 s[44:45], s[82:83], 13
	v_lshlrev_b32_e32 v64, 7, v127
	v_or_b32_e32 v6, s44, v64
	v_mov_b32_e32 v7, s45
	v_lshl_add_u64 v[6:7], s[26:27], 0, v[6:7]
	v_lshl_add_u64 v[6:7], v[6:7], 0, v[2:3]
	s_mov_b64 s[26:27], 0x7e00000
	v_lshl_add_u64 v[134:135], v[6:7], 0, s[26:27]
	s_mov_b64 s[26:27], 0x7e10000
	v_lshl_add_u64 v[136:137], v[6:7], 0, s[26:27]
	s_mov_b64 s[26:27], 0x7e10040
	v_and_b32_e32 v128, -16, v4
	v_lshl_add_u64 v[138:139], v[6:7], 0, s[26:27]
	s_movk_i32 s26, 0x1c0
	v_add_u32_e32 v0, s4, v128
	v_mad_u32_u24 v6, v127, s26, v9
	s_lshl_b32 s26, s4, 1
	v_add3_u32 v183, v6, s26, v128
	v_lshl_add_u32 v184, v1, 2, s4
	v_lshlrev_b32_e32 v1, 2, v0
	v_readlane_b32 s26, v254, 56
	s_mov_b32 s70, s91
	s_mov_b32 s71, s93
	s_movk_i32 s72, 0x3ff
	s_cmpk_lg_u32 s91, 0x100
	s_cbranch_scc1 .Lprep_nomap
	s_movk_i32 s70, 0x20
	s_lshr_b32 s71, s93, 5
	s_lshl_b32 s71, s71, 7
	s_and_b32 s72, s93, 31
	s_add_i32 s71, s71, s72
	s_or_b32 s72, s71, 0x7f
.Lprep_nomap:
	s_lshl_b32 s33, s70, 4
	s_add_u32 s62, s6, 0x48000400
	v_add_u32_e32 v187, s26, v1
	s_movk_i32 s26, 0x400
	v_cmp_gt_i32_e64 s[42:43], s26, v126
	s_addc_u32 s63, s7, 0
	v_readlane_b32 s26, v254, 54
	v_add_u32_e32 v186, 0, v1
	v_lshlrev_b32_e32 v1, 3, v4
	v_readlane_b32 s27, v254, 55
	s_add_u32 s26, s26, s44
	v_lshl_add_u32 v191, s82, 9, v1
	v_ashrrev_i32_e32 v1, 31, v0
	s_addc_u32 s27, s27, s45
	v_lshlrev_b64 v[140:141], 1, v[0:1]
	v_lshl_add_u64 v[0:1], s[26:27], 0, v[64:65]
	v_ashrrev_i32_e32 v129, 31, v128
	v_and_b32_e32 v8, 3, v4
	v_lshl_add_u64 v[0:1], v[0:1], 0, v[2:3]
	v_add_u32_e32 v182, v9, v128
	v_cmp_gt_u32_e64 s[38:39], 16, v4
	v_lshl_add_u64 v[132:133], v[128:129], 0, s[4:5]
	v_lshl_add_u32 v185, v127, 10, v6
	v_add_u32_e32 v188, 16, v187
	v_add_u32_e32 v189, 32, v187
	v_add_u32_e32 v190, 48, v187
	v_cmp_gt_i32_e64 s[40:41], s31, v126
	v_lshl_or_b32 v142, s71, 4, v127
	v_add3_u32 v192, s4, v5, v8
	v_lshl_add_u64 v[144:145], s[6:7], 0, v[0:1]
	s_mov_b32 s34, s71
	v_readlane_b32 s69, v254, 57

.LBB0_896:
	s_waitcnt vmcnt(3) lgkmcnt(1)
	v_mfma_f32_16x16x32_bf16 v[36:39], v[36:39], v[0:3], 0
	v_add_u32_e32 v52, s27, v184
	s_add_i32 s26, s26, 16
	s_add_u32 s48, s48, 0x800
	s_waitcnt vmcnt(1)
	v_mfma_f32_16x16x32_bf16 v[32:35], v[32:35], v[0:3], 0
	s_addc_u32 s49, s49, 0
	s_cmpk_eq_i32 s48, 0x2000
	s_waitcnt lgkmcnt(0)
	v_mfma_f32_16x16x32_bf16 v[40:43], v[28:31], v[4:7], v[36:39]
	s_waitcnt vmcnt(0)
	v_mfma_f32_16x16x32_bf16 v[28:31], v[24:27], v[4:7], v[32:35]
	v_lshlrev_b32_e32 v24, 2, v52
	v_add_u32_e32 v25, 0, v24
	v_add_u32_e32 v26, 0x13200, v25
	ds_read_b128 v[44:47], v26
	v_add_u32_e32 v26, 0x13a00, v25
	ds_read_b128 v[36:39], v26
	v_add_u32_e32 v25, 0x14200, v25
	ds_read_b128 v[32:35], v25
	s_waitcnt lgkmcnt(2)
	v_add_f32_e32 v40, v40, v44
	v_mul_f32_e32 v40, 0xbfb8aa3b, v40
	s_waitcnt lgkmcnt(1)
	v_add_f32_e32 v28, v28, v36
	v_mul_f32_e32 v28, 0xbfb8aa3b, v28
	v_exp_f32_e32 v28, v28
	v_add_f32_e32 v29, v29, v37
	v_mul_f32_e32 v29, 0xbfb8aa3b, v29
	v_exp_f32_e32 v29, v29
	v_add_f32_e32 v28, 1.0, v28
	v_rcp_f32_e32 v28, v28
	v_exp_f32_e32 v40, v40
	v_add_f32_e32 v29, 1.0, v29
	v_rcp_f32_e32 v29, v29
	s_waitcnt lgkmcnt(0)
	v_mul_f32_e32 v32, v32, v28
	v_mul_f32_e32 v28, 0x3fb8aa3b, v32
	v_add_f32_e32 v32, v32, v32
	v_mul_f32_e32 v32, 0x3fb8aa3b, v32
	v_exp_f32_e32 v32, v32
	v_mul_f32_e32 v33, v33, v29
	v_mul_f32_e32 v29, 0x3fb8aa3b, v33
	v_add_f32_e32 v33, v33, v33
	v_sub_f32_e32 v32, 1.0, v32
	v_cmp_gt_f32_e32 vcc, s29, v32
	v_mul_f32_e32 v36, 0x4f800000, v32
	v_mul_f32_e32 v33, 0x3fb8aa3b, v33
	v_cndmask_b32_e32 v32, v32, v36, vcc
	v_sqrt_f32_e32 v36, v32
	v_exp_f32_e32 v33, v33
	v_add_u32_e32 v24, v185, v24
	v_add_f32_e32 v40, 1.0, v40
	v_add_u32_e32 v44, -1, v36
	v_fma_f32 v53, -v44, v36, v32
	v_cmp_ge_f32_e64 s[46:47], 0, v53
	v_add_u32_e32 v53, 1, v36
	v_sub_f32_e32 v33, 1.0, v33
	v_cndmask_b32_e64 v44, v36, v44, s[46:47]
	v_fma_f32 v36, -v53, v36, v32
	v_cmp_lt_f32_e64 s[46:47], 0, v36
	ds_read_b128 v[24:27], v24 offset:26624
	v_rcp_f32_e32 v40, v40
	v_cndmask_b32_e64 v36, v44, v53, s[46:47]
	v_mul_f32_e32 v44, 0x37800000, v36
	v_cndmask_b32_e32 v36, v36, v44, vcc
	v_cmp_class_f32_e32 vcc, v32, v214
	v_exp_f32_e32 v28, v28
	v_exp_f32_e32 v29, v29
	v_cndmask_b32_e32 v32, v36, v32, vcc
	v_cmp_gt_f32_e32 vcc, s29, v33
	v_mul_f32_e32 v36, 0x4f800000, v33
	v_cndmask_b32_e64 v32, v32, 1.0, s[44:45]
	v_cndmask_b32_e32 v33, v33, v36, vcc
	v_sqrt_f32_e32 v36, v33
	v_mul_f32_e32 v32, v40, v32
	s_waitcnt lgkmcnt(0)
	v_mul_f32_e32 v32, v24, v32
	v_add_f32_e32 v24, v41, v45
	v_mul_f32_e32 v24, 0xbfb8aa3b, v24
	v_add_u32_e32 v37, -1, v36
	v_exp_f32_e32 v24, v24
	v_fma_f32 v40, -v37, v36, v33
	v_cmp_ge_f32_e64 s[46:47], 0, v40
	v_add_u32_e32 v40, 1, v36
	v_add_f32_e32 v24, 1.0, v24
	v_cndmask_b32_e64 v37, v36, v37, s[46:47]
	v_fma_f32 v36, -v40, v36, v33
	v_cmp_lt_f32_e64 s[46:47], 0, v36
	v_rcp_f32_e32 v24, v24
	v_ashrrev_i32_e32 v53, 31, v52
	v_cndmask_b32_e64 v36, v37, v40, s[46:47]
	v_mul_f32_e32 v37, 0x37800000, v36
	v_cndmask_b32_e32 v36, v36, v37, vcc
	v_cmp_class_f32_e32 vcc, v33, v214
	s_nop 1
	v_cndmask_b32_e32 v33, v36, v33, vcc
	v_cndmask_b32_e64 v33, v33, 1.0, s[44:45]
	v_mul_f32_e32 v24, v24, v33
	v_mul_f32_e32 v33, v25, v24
	v_add_f32_e32 v25, v30, v38
	v_mul_f32_e32 v25, 0xbfb8aa3b, v25
	v_exp_f32_e32 v25, v25
	v_add_f32_e32 v24, v42, v46
	v_mul_f32_e32 v24, 0xbfb8aa3b, v24
	v_exp_f32_e32 v24, v24
	v_add_f32_e32 v25, 1.0, v25
	v_rcp_f32_e32 v25, v25
	v_add_f32_e32 v24, 1.0, v24
	v_rcp_f32_e32 v24, v24
	v_mul_f32_e32 v25, v34, v25
	v_mul_f32_e32 v30, 0x3fb8aa3b, v25
	v_add_f32_e32 v25, v25, v25
	v_mul_f32_e32 v25, 0x3fb8aa3b, v25
	v_exp_f32_e32 v25, v25
	v_exp_f32_e32 v30, v30
	v_sub_f32_e32 v25, 1.0, v25
	v_cmp_gt_f32_e32 vcc, s29, v25
	v_mul_f32_e32 v34, 0x4f800000, v25
	s_nop 0
	v_cndmask_b32_e32 v25, v25, v34, vcc
	v_sqrt_f32_e32 v34, v25
	s_nop 0
	v_add_u32_e32 v36, -1, v34
	v_fma_f32 v37, -v36, v34, v25
	v_cmp_ge_f32_e64 s[46:47], 0, v37
	v_add_u32_e32 v37, 1, v34
	s_nop 0
	v_cndmask_b32_e64 v36, v34, v36, s[46:47]
	v_fma_f32 v34, -v37, v34, v25
	v_cmp_lt_f32_e64 s[46:47], 0, v34
	s_nop 1
	v_cndmask_b32_e64 v34, v36, v37, s[46:47]
	v_mul_f32_e32 v36, 0x37800000, v34
	v_cndmask_b32_e32 v34, v34, v36, vcc
	v_cmp_class_f32_e32 vcc, v25, v214
	s_nop 1
	v_cndmask_b32_e32 v25, v34, v25, vcc
	v_cndmask_b32_e64 v25, v25, 1.0, s[44:45]
	v_mul_f32_e32 v24, v24, v25
	v_add_f32_e32 v25, v31, v39
	v_mul_f32_e32 v25, 0xbfb8aa3b, v25
	v_exp_f32_e32 v25, v25
	v_mul_f32_e32 v26, v26, v24
	v_add_f32_e32 v24, v43, v47
	v_mul_f32_e32 v24, 0xbfb8aa3b, v24
	v_add_f32_e32 v25, 1.0, v25
	v_rcp_f32_e32 v25, v25
	v_exp_f32_e32 v24, v24
	v_mul_f32_e32 v25, v35, v25
	v_mul_f32_e32 v31, 0x3fb8aa3b, v25
	v_add_f32_e32 v25, v25, v25
	v_mul_f32_e32 v25, 0x3fb8aa3b, v25
	v_exp_f32_e32 v25, v25
	v_add_f32_e32 v24, 1.0, v24
	v_rcp_f32_e32 v24, v24
	v_exp_f32_e32 v31, v31
	v_sub_f32_e32 v25, 1.0, v25
	v_cmp_gt_f32_e32 vcc, s29, v25
	v_mul_f32_e32 v34, 0x4f800000, v25
	s_nop 0
	v_cndmask_b32_e32 v25, v25, v34, vcc
	v_sqrt_f32_e32 v34, v25
	s_nop 0
	v_add_u32_e32 v35, -1, v34
	v_fma_f32 v36, -v35, v34, v25
	v_cmp_ge_f32_e64 s[46:47], 0, v36
	v_add_u32_e32 v36, 1, v34
	s_nop 0
	v_cndmask_b32_e64 v35, v34, v35, s[46:47]
	v_fma_f32 v34, -v36, v34, v25
	v_cmp_lt_f32_e64 s[46:47], 0, v34
	s_nop 1
	v_cndmask_b32_e64 v34, v35, v36, s[46:47]
	v_mul_f32_e32 v35, 0x37800000, v34
	v_cndmask_b32_e32 v34, v34, v35, vcc
	v_cmp_class_f32_e32 vcc, v25, v214
	s_nop 1
	v_cndmask_b32_e32 v25, v34, v25, vcc
	v_cndmask_b32_e64 v25, v25, 1.0, s[44:45]
	v_mul_f32_e32 v24, v24, v25
	v_mul_f32_e32 v27, v27, v24
	v_lshl_add_u64 v[24:25], v[52:53], 2, v[48:49]
	global_store_dwordx4 v[24:25], v[28:31], off
	v_cvt_pk_bf16_f32 v24, v32, v33
	v_cvt_pk_bf16_f32 v25, v26, v27
	v_lshl_add_u64 v[26:27], v[52:53], 1, v[50:51]
	global_store_dwordx2 v[26:27], v[24:25], off
	s_cbranch_scc0 .LBB0_894
	s_add_i32 s34, s34, s70
	s_cmp_gt_i32 s34, s72
	v_add_u32_e32 v142, s33, v142
	s_barrier
	s_cbranch_scc0 .LBB0_823
	v_readlane_b32 s83, v255, 1

.LBB0_1643:
	s_andn2_b64 vcc, exec, s[4:5]
	s_cbranch_vccnz .LBB0_1702
	s_lshl_b32 s26, s91, 3
	s_abs_i32 s4, s26
	s_waitcnt vmcnt(0)
	v_cvt_f32_u32_e32 v0, s4
	s_lshl_b32 s5, s93, 3
	s_add_i32 s22, s5, s82
	s_sub_i32 s5, s26, s22
	v_rcp_iflag_f32_e32 v0, v0
	s_add_i32 s7, s5, 0x3fff
	s_sub_i32 s5, 0xffffc001, s5
	s_xor_b32 s8, s7, s26
	v_mul_f32_e32 v0, 0x4f7ffffe, v0
	v_cvt_u32_f32_e32 v0, v0
	s_sub_i32 s6, 0, s4
	s_max_i32 s5, s7, s5
	s_ashr_i32 s7, s8, 31
	v_readfirstlane_b32 s8, v0
	s_mul_i32 s6, s6, s8
	s_mul_hi_u32 s6, s8, s6
	s_add_i32 s8, s8, s6
	s_mul_hi_u32 s6, s5, s8
	s_mul_i32 s8, s6, s4
	s_sub_i32 s5, s5, s8
	s_add_i32 s8, s6, 1
	s_sub_i32 s9, s5, s4
	s_cmp_ge_u32 s5, s4
	s_cselect_b32 s6, s8, s6
	s_cselect_b32 s5, s9, s5
	s_add_i32 s8, s6, 1
	s_cmp_ge_u32 s5, s4
	s_cselect_b32 s4, s8, s6
	s_xor_b32 s4, s4, s7
	s_sub_i32 s27, s4, s7
	s_cmpk_lg_u32 s91, 0x100
	s_cbranch_scc1 .Lpost_nomap
	s_lshr_b32 s4, s93, 5
	s_and_b32 s5, s93, 31
	s_lshl_b32 s4, s4, 11
	s_lshl_b32 s5, s5, 3
	s_add_i32 s22, s4, s5
	s_add_i32 s22, s22, s82
	s_movk_i32 s26, 0x100
	s_mov_b32 s27, 8
.Lpost_nomap:
	s_cmp_lt_i32 s27, 1
	s_cbranch_scc1 .LBB0_1651
	s_load_dwordx2 s[18:19], s[16:17], 0x170
	s_load_dwordx2 s[24:25], s[16:17], 0xb8
	v_readlane_b32 s38, v255, 4
	v_readlane_b32 s39, v255, 5
	v_lshlrev_b32_e32 v90, 3, v32
	s_waitcnt lgkmcnt(0)
	s_add_u32 s33, s18, 0x48000000
	s_addc_u32 s40, s19, 0
	s_add_u32 s4, s18, 0x72200000
	s_addc_u32 s5, s19, 0
	s_add_u32 s6, s18, 0x74200000
	s_addc_u32 s7, s19, 0
	s_add_u32 s8, s18, 0x76200000
	s_addc_u32 s9, s19, 0
	s_add_u32 s10, s18, 0x78200000
	s_addc_u32 s11, s19, 0
	s_add_u32 s12, s18, 0x63000000
	s_addc_u32 s13, s19, 0
	s_add_u32 s14, s18, 0x60000000
	s_addc_u32 s15, s19, 0
	s_add_u32 s20, s18, 0x6c000000
	s_addc_u32 s21, s19, 0
	s_lshl_b32 s34, s38, 9
	s_lshl_b64 s[38:39], s[34:35], 2
	v_ashrrev_i32_e32 v91, 31, v90
	s_add_u32 s24, s24, s38
	s_addc_u32 s25, s25, s39
	v_lshlrev_b64 v[24:25], 2, v[90:91]
	v_lshl_add_u64 v[4:5], s[24:25], 0, v[24:25]
	global_load_dwordx4 v[0:3], v[4:5], off
	s_nop 0
	global_load_dwordx4 v[4:7], v[4:5], off offset:16
	s_load_dwordx4 s[44:47], s[16:17], 0x78
	s_nop 0
	s_load_dwordx2 s[16:17], s[16:17], 0x90
	v_ashrrev_i32_e32 v32, 3, v32
	v_ashrrev_i32_e32 v33, 31, v32
	v_lshlrev_b64 v[32:33], 2, v[32:33]
	s_mov_b32 s34, 0
	s_waitcnt lgkmcnt(0)
	s_add_u32 s16, s16, s38
	s_addc_u32 s17, s17, s39
	v_lshl_add_u64 v[12:13], s[16:17], 0, v[24:25]
	s_add_u32 s16, s46, s38
	s_addc_u32 s17, s47, s39
	v_lshl_add_u64 v[20:21], s[16:17], 0, v[24:25]
	s_add_u32 s16, s44, s38
	s_addc_u32 s17, s45, s39
	s_ashr_i32 s23, s22, 31
	v_lshl_add_u64 v[28:29], s[16:17], 0, v[24:25]
	s_lshl_b64 s[16:17], s[22:23], 5
	s_add_u32 s16, s20, s16
	s_addc_u32 s17, s21, s17
	v_lshl_add_u64 v[34:35], s[16:17], 0, v[32:33]
	s_mul_i32 s16, s22, 0x5800
	s_mul_hi_i32 s17, s22, 0x5800
	s_add_u32 s16, s33, s16
	s_addc_u32 s17, s40, s17
	global_load_dwordx4 v[8:11], v[12:13], off
	s_nop 0
	global_load_dwordx4 v[12:15], v[12:13], off offset:16
	s_nop 0
	global_load_dwordx4 v[16:19], v[20:21], off
	s_nop 0
	global_load_dwordx4 v[20:23], v[20:21], off offset:16
	s_nop 0
	global_load_dwordx4 v[24:27], v[28:29], off
	s_nop 0
	global_load_dwordx4 v[28:31], v[28:29], off offset:16
	v_lshl_add_u64 v[94:95], s[20:21], 0, v[32:33]
	global_load_dword v92, v[34:35], off
	v_lshl_add_u64 v[34:35], v[90:91], 1, s[16:17]
	s_movk_i32 s16, 0x2000
	v_add_co_u32_e32 v36, vcc, s16, v34
	s_movk_i32 s16, 0x1000
	s_nop 0
	v_addc_co_u32_e32 v37, vcc, 0, v35, vcc
	v_add_co_u32_e32 v34, vcc, s16, v34
	s_lshl_b64 s[16:17], s[22:23], 9
	s_nop 0
	v_addc_co_u32_e32 v35, vcc, 0, v35, vcc
	global_load_dwordx4 v[60:63], v[36:37], off offset:2560
	global_load_dwordx4 v[70:73], v[34:35], off offset:2560
	v_lshl_add_u64 v[34:35], s[16:17], 0, v[90:91]
	v_lshlrev_b64 v[34:35], 1, v[34:35]
	v_lshl_add_u64 v[36:37], s[14:15], 0, v[34:35]
	global_load_dwordx4 v[78:81], v[36:37], off
	v_lshl_add_u64 v[36:37], s[12:13], 0, v[34:35]
	global_load_dwordx4 v[82:85], v[36:37], off
	v_lshl_add_u64 v[36:37], s[8:9], 0, v[34:35]
	global_load_dwordx4 v[66:69], v[36:37], off nt
	v_lshl_add_u64 v[36:37], s[6:7], 0, v[34:35]
	v_lshl_add_u64 v[34:35], s[4:5], 0, v[34:35]
	global_load_dwordx4 v[74:77], v[36:37], off nt
	global_load_dwordx4 v[86:89], v[34:35], off nt
	s_add_u32 s16, s18, 0x78a00000
	s_addc_u32 s17, s19, 0
	s_add_u32 s18, s18, 0x79200000
	s_addc_u32 s19, s19, 0
	s_waitcnt vmcnt(9)
	v_mov_b32_e32 v101, v26
	s_waitcnt vmcnt(8)
	v_mov_b32_e32 v97, v30
	v_mov_b32_e32 v99, v28
	v_mov_b32_e32 v93, v24
	s_branch .LBB0_1647

.LBB0_1682:
	s_andn2_saveexec_b64 s[6:7], s[6:7]
	s_cbranch_execz .LBB0_1701
	s_mov_b64 s[6:7], exec
	s_waitcnt lgkmcnt(0)
	s_branch .Lxl_1702
	s_waitcnt lgkmcnt(0)
	s_waitcnt vmcnt(0)
	v_mbcnt_lo_u32_b32 v1, s6, 0
	v_mbcnt_hi_u32_b32 v1, s7, v1
	v_cmp_eq_u32_e32 vcc, 0, v1
	s_and_saveexec_b64 s[8:9], vcc
	s_cbranch_execz .LBB0_1685
	s_bcnt1_i32_b64 s6, s[6:7]
	v_mov_b32_e32 v2, s6
	v_readlane_b32 s6, v254, 21
	v_readlane_b32 s7, v254, 22
	s_nop 4
	global_atomic_add v2, v65, v2, s[6:7] sc0

.Lxl_1702:
	v_readlane_b32 s6, v254, 19
	v_readlane_b32 s7, v254, 20
	s_waitcnt vmcnt(0)
	s_nop 3
	global_atomic_add v65, v167, s[6:7]
	s_waitcnt vmcnt(0)
